# speedup vs baseline: 1.0140x; 1.0140x over previous
.LBB2_4:
	s_or_saveexec_b64 s[48:49], s[4:5]
	s_load_dwordx4 s[40:43], s[0:1], 0x20
	v_and_b32_e32 v140, 31, v0
	v_bfe_u32 v139, v0, 5, 1
	s_xor_b64 exec, exec, s[48:49]
	s_cbranch_execz .LBB2_20
	s_setprio 2
	v_or_b32_e32 v116, s52, v116
	s_nop 3
	v_lshlrev_b64 v[2:3], 12, v[116:117]
	v_lshl_add_u64 v[2:3], s[44:45], 0, v[2:3]
	v_mov_b32_e32 v131, 0
	v_lshl_add_u64 v[2:3], v[2:3], 0, v[130:131]
	global_load_dwordx4 v[50:53], v[2:3], off
	global_load_dwordx4 v[54:57], v[2:3], off offset:1024
	global_load_dwordx4 v[58:61], v[2:3], off offset:2048
	global_load_dwordx4 v[62:65], v[2:3], off offset:3072
	global_load_dwordx4 v[98:101], v[114:115], off offset:3072
	global_load_dwordx4 v[102:105], v[114:115], off offset:2048
	global_load_dwordx4 v[106:109], v[114:115], off offset:1024
	global_load_dwordx4 v[34:37], v[114:115], off
	v_lshlrev_b32_e32 v2, 2, v139
	v_or_b32_e32 v3, 2, v2
	v_cmp_gt_u32_e64 s[8:9], v3, v140
	v_or_b32_e32 v3, 3, v2
	v_cmp_gt_u32_e64 s[10:11], v3, v140
	v_or_b32_e32 v3, 8, v2
	v_cmp_gt_u32_e64 s[12:13], v3, v140
	v_or_b32_e32 v3, 9, v2
	v_cmp_gt_u32_e64 s[14:15], v3, v140
	v_or_b32_e32 v3, 10, v2
	v_cmp_gt_u32_e64 s[16:17], v3, v140
	v_or_b32_e32 v3, 11, v2
	v_cmp_gt_u32_e64 s[18:19], v3, v140
	v_or_b32_e32 v3, 16, v2
	v_cmp_gt_u32_e64 s[20:21], v3, v140
	v_or_b32_e32 v3, 17, v2
	v_cmp_gt_u32_e64 s[22:23], v3, v140
	v_or_b32_e32 v3, 18, v2
	v_cmp_gt_u32_e64 s[24:25], v3, v140
	v_or_b32_e32 v3, 19, v2
	s_lshl_b32 s2, s2, 9
	v_cmp_gt_u32_e64 s[26:27], v3, v140
	v_or_b32_e32 v3, 24, v2
	s_and_b32 s54, s2, 0x3000
	s_lshr_b32 s2, s3, 3
	v_cmp_gt_u32_e64 s[28:29], v3, v140
	v_or_b32_e32 v3, 25, v2
	s_mul_i32 s2, s2, 48
	v_cmp_gt_u32_e64 s[4:5], v2, v140
	v_cmp_lt_u32_e64 s[6:7], v2, v140
	v_cmp_gt_u32_e64 s[30:31], v3, v140
	v_or_b32_e32 v3, 26, v2
	v_or_b32_e32 v2, 27, v2
	s_add_i32 s2, s2, s53
	v_cmp_gt_u32_e64 s[36:37], v2, v140
	v_add_u32_e32 v2, s2, v132
	v_cmp_gt_u32_e64 s[34:35], v3, v140
	v_ashrrev_i32_e32 v3, 31, v2
	v_lshlrev_b64 v[2:3], 15, v[2:3]
	v_or_b32_e32 v2, v2, v130
	s_mov_b32 s55, 0
	v_lshl_add_u64 v[110:111], s[46:47], 0, v[2:3]
	s_add_u32 s46, s54, 0x1000
	v_lshl_add_u64 v[112:113], s[50:51], 0, v[2:3]
	v_mov_b32_e32 v116, 0xff800000
	s_mov_b64 s[2:3], 0
	v_mov_b32_e32 v119, 0xff800000
	v_mov_b32_e32 v2, v131
	v_mov_b32_e32 v3, v131
	v_mov_b32_e32 v4, v131
	v_mov_b32_e32 v5, v131
	v_mov_b32_e32 v6, v131
	v_mov_b32_e32 v7, v131
	v_mov_b32_e32 v8, v131
	v_mov_b32_e32 v9, v131
	v_mov_b32_e32 v10, v131
	v_mov_b32_e32 v11, v131
	v_mov_b32_e32 v12, v131
	v_mov_b32_e32 v13, v131
	v_mov_b32_e32 v14, v131
	v_mov_b32_e32 v15, v131
	v_mov_b32_e32 v16, v131
	v_mov_b32_e32 v17, v131
	v_mov_b32_e32 v18, v131
	v_mov_b32_e32 v19, v131
	v_mov_b32_e32 v20, v131
	v_mov_b32_e32 v21, v131
	v_mov_b32_e32 v22, v131
	v_mov_b32_e32 v23, v131
	v_mov_b32_e32 v24, v131
	v_mov_b32_e32 v25, v131
	v_mov_b32_e32 v26, v131
	v_mov_b32_e32 v27, v131
	v_mov_b32_e32 v28, v131
	v_mov_b32_e32 v29, v131
	v_mov_b32_e32 v30, v131
	s_waitcnt vmcnt(3)
	v_mov_b64_e32 v[66:67], v[98:99]
	s_waitcnt vmcnt(2)
	v_mov_b64_e32 v[70:71], v[102:103]
	s_waitcnt vmcnt(1)
	v_mov_b64_e32 v[74:75], v[106:107]
	s_waitcnt vmcnt(0)
	v_mov_b64_e32 v[80:81], v[36:37]
	v_mov_b32_e32 v31, v131
	v_mov_b32_e32 v32, v131
	v_mov_b32_e32 v33, v131
	v_mov_b64_e32 v[68:69], v[100:101]
	v_mov_b64_e32 v[72:73], v[104:105]
	v_mov_b64_e32 v[76:77], v[108:109]
	v_mov_b64_e32 v[78:79], v[34:35]

.LBB2_8:
	s_setprio 3
	v_mfma_f32_32x32x16_f16 v[34:49], v[34:37], v[50:53], 0
	v_mfma_f32_32x32x16_f16 v[34:49], v[106:109], v[54:57], v[34:49]
	v_mfma_f32_32x32x16_f16 v[34:49], v[102:105], v[58:61], v[34:49]
	v_mfma_f32_32x32x16_f16 v[34:49], v[98:101], v[62:65], v[34:49]
	s_setprio 2
	s_cmp_lg_u32 s54, s2
	s_cbranch_scc1 .LBB2_10
	s_nop 8
	v_cndmask_b32_e64 v98, v34, v116, s[4:5]
	v_cndmask_b32_e64 v35, v116, v35, s[6:7]
	v_cndmask_b32_e64 v34, v98, v34, s[6:7]
	v_cndmask_b32_e64 v36, v36, v116, s[8:9]
	v_cndmask_b32_e64 v37, v37, v116, s[10:11]
	v_cndmask_b32_e64 v38, v38, v116, s[12:13]
	v_cndmask_b32_e64 v39, v39, v116, s[14:15]
	v_cndmask_b32_e64 v40, v40, v116, s[16:17]
	v_cndmask_b32_e64 v41, v41, v116, s[18:19]
	v_cndmask_b32_e64 v42, v42, v116, s[20:21]
	v_cndmask_b32_e64 v43, v43, v116, s[22:23]
	v_cndmask_b32_e64 v44, v44, v116, s[24:25]
	v_cndmask_b32_e64 v45, v45, v116, s[26:27]
	v_cndmask_b32_e64 v46, v46, v116, s[28:29]
	v_cndmask_b32_e64 v47, v47, v116, s[30:31]
	v_cndmask_b32_e64 v48, v48, v116, s[34:35]
	v_cndmask_b32_e64 v49, v49, v116, s[36:37]
.LBB2_10:
	s_nop 8
	v_max_f32_e32 v98, v35, v35
	v_max_f32_e32 v99, v34, v34
	v_max_f32_e32 v98, v99, v98
	v_max3_f32 v98, v98, v36, v37
	v_max3_f32 v98, v98, v38, v39
	v_max3_f32 v98, v98, v40, v41
	v_max3_f32 v98, v98, v42, v43
	v_max3_f32 v98, v98, v44, v45
	v_max3_f32 v98, v98, v46, v47
	v_max3_f32 v98, v98, v48, v49
	ds_bpermute_b32 v99, v138, v98
	s_waitcnt lgkmcnt(0)
	v_max3_f32 v98, v119, v98, v99
	v_sub_f32_e32 v34, v34, v98
	v_sub_f32_e32 v35, v35, v98
	v_exp_f32_e32 v100, v34
	v_exp_f32_e32 v35, v35
	v_sub_f32_e32 v36, v36, v98
	v_sub_f32_e32 v34, v37, v98
	v_exp_f32_e32 v37, v36
	v_add_f32_e32 v36, 0, v100
	v_exp_f32_e32 v101, v34
	v_sub_f32_e32 v34, v38, v98
	v_exp_f32_e32 v38, v34
	v_add_f32_e32 v34, v35, v36
	v_sub_f32_e32 v36, v39, v98
	v_exp_f32_e32 v102, v36
	v_sub_f32_e32 v36, v40, v98
	v_add_f32_e32 v34, v37, v34
	v_exp_f32_e32 v39, v36
	v_sub_f32_e32 v36, v41, v98
	v_add_f32_e32 v34, v101, v34
	v_exp_f32_e32 v40, v36
	v_sub_f32_e32 v36, v42, v98
	v_add_f32_e32 v34, v38, v34
	v_exp_f32_e32 v103, v36
	v_sub_f32_e32 v36, v43, v98
	v_add_f32_e32 v34, v102, v34
	v_exp_f32_e32 v104, v36
	v_sub_f32_e32 v36, v44, v98
	v_add_f32_e32 v34, v39, v34
	v_exp_f32_e32 v41, v36
	v_sub_f32_e32 v36, v45, v98
	v_add_f32_e32 v34, v40, v34
	v_exp_f32_e32 v44, v36
	v_sub_f32_e32 v36, v46, v98
	v_add_f32_e32 v34, v103, v34
	v_exp_f32_e32 v42, v36
	v_sub_f32_e32 v36, v47, v98
	v_add_f32_e32 v34, v104, v34
	v_exp_f32_e32 v45, v36
	v_sub_f32_e32 v36, v48, v98
	v_add_f32_e32 v34, v41, v34
	v_exp_f32_e32 v43, v36
	v_sub_f32_e32 v36, v49, v98
	v_sub_f32_e32 v99, v119, v98
	v_add_f32_e32 v34, v44, v34
	v_exp_f32_e32 v46, v36
	v_add_f32_e32 v34, v42, v34
	v_exp_f32_e32 v36, v99
	v_add_f32_e32 v34, v45, v34
	v_add_f32_e32 v34, v43, v34
	v_add_f32_e32 v34, v46, v34
	v_fmac_f32_e32 v34, v131, v36
	v_mul_f32_e32 v32, v36, v32
	v_mul_f32_e32 v33, v36, v33
	v_mul_f32_e32 v30, v36, v30
	v_mul_f32_e32 v31, v36, v31
	v_mul_f32_e32 v28, v36, v28
	v_mul_f32_e32 v29, v36, v29
	v_mul_f32_e32 v26, v36, v26
	v_mul_f32_e32 v27, v36, v27
	v_mul_f32_e32 v24, v36, v24
	v_mul_f32_e32 v25, v36, v25
	v_mul_f32_e32 v22, v36, v22
	v_mul_f32_e32 v23, v36, v23
	v_mul_f32_e32 v20, v36, v20
	v_mul_f32_e32 v21, v36, v21
	v_mul_f32_e32 v18, v36, v18
	v_mul_f32_e32 v19, v36, v19
	v_mul_f32_e32 v16, v36, v16
	v_mul_f32_e32 v17, v36, v17
	v_mul_f32_e32 v14, v36, v14
	v_mul_f32_e32 v15, v36, v15
	v_mul_f32_e32 v12, v36, v12
	v_mul_f32_e32 v13, v36, v13
	v_mul_f32_e32 v10, v36, v10
	v_mul_f32_e32 v11, v36, v11
	v_mul_f32_e32 v8, v36, v8
	v_mul_f32_e32 v9, v36, v9
	v_mul_f32_e32 v6, v36, v6
	v_mul_f32_e32 v7, v36, v7
	v_mul_f32_e32 v4, v36, v4
	v_mul_f32_e32 v5, v36, v5
	v_mul_f32_e32 v2, v36, v2
	v_mul_f32_e32 v3, v36, v3
	v_cvt_pk_f16_f32 v39, v39, v40
	v_cvt_pk_f16_f32 v38, v38, v102
	v_cvt_pk_f16_f32 v37, v37, v101
	v_cvt_pk_f16_f32 v36, v100, v35
	v_cvt_pk_f16_f32 v43, v43, v46
	v_cvt_pk_f16_f32 v42, v42, v45
	v_cvt_pk_f16_f32 v41, v41, v44
	v_cvt_pk_f16_f32 v40, v103, v104
	s_setprio 3
	s_waitcnt vmcnt(3)
	v_mfma_f32_32x32x16_f16 v[18:33], v[94:97], v[36:39], v[18:33]
	s_waitcnt vmcnt(1)
	v_mfma_f32_32x32x16_f16 v[2:17], v[86:89], v[36:39], v[2:17]
	v_mfma_f32_32x32x16_f16 v[18:33], v[90:93], v[40:43], v[18:33]
	s_waitcnt vmcnt(0)
	v_mfma_f32_32x32x16_f16 v[2:17], v[82:85], v[40:43], v[2:17]
	s_setprio 2
	s_add_i32 s55, s55, 1
	s_add_u32 s2, s2, 0x1000
	s_addc_u32 s3, s3, 0
	s_cmp_lg_u32 s46, s2
	s_cbranch_scc0 .LBB2_12
	v_mov_b32_e32 v119, v98
	v_mov_b32_e32 v131, v34
	v_mov_b64_e32 v[100:101], v[68:69]
	v_mov_b64_e32 v[104:105], v[72:73]
	v_mov_b64_e32 v[108:109], v[76:77]
	v_mov_b64_e32 v[34:35], v[78:79]
	v_mov_b64_e32 v[98:99], v[66:67]
	v_mov_b64_e32 v[102:103], v[70:71]
	v_mov_b64_e32 v[106:107], v[74:75]
	v_mov_b64_e32 v[36:37], v[80:81]
	s_branch .LBB2_6

.LBB2_15:
	s_setprio 3
	v_mfma_f32_32x32x16_f16 v[34:49], v[34:37], v[50:53], 0
	v_mfma_f32_32x32x16_f16 v[34:49], v[106:109], v[54:57], v[34:49]
	s_waitcnt vmcnt(5)
	v_mfma_f32_32x32x16_f16 v[34:49], v[102:105], v[58:61], v[34:49]
	s_waitcnt vmcnt(4)
	v_mfma_f32_32x32x16_f16 v[34:49], v[98:101], v[62:65], v[34:49]
	s_setprio 2
	s_cmp_lg_u32 s47, s2
	s_cbranch_scc1 .LBB2_17
	s_nop 8
	v_cndmask_b32_e64 v98, v34, v114, s[4:5]
	v_cndmask_b32_e64 v35, v114, v35, s[6:7]
	v_cndmask_b32_e64 v34, v98, v34, s[6:7]
	v_cndmask_b32_e64 v36, v36, v114, s[8:9]
	v_cndmask_b32_e64 v37, v37, v114, s[10:11]
	v_cndmask_b32_e64 v38, v38, v114, s[12:13]
	v_cndmask_b32_e64 v39, v39, v114, s[14:15]
	v_cndmask_b32_e64 v40, v40, v114, s[16:17]
	v_cndmask_b32_e64 v41, v41, v114, s[18:19]
	v_cndmask_b32_e64 v42, v42, v114, s[20:21]
	v_cndmask_b32_e64 v43, v43, v114, s[22:23]
	v_cndmask_b32_e64 v44, v44, v114, s[24:25]
	v_cndmask_b32_e64 v45, v45, v114, s[26:27]
	v_cndmask_b32_e64 v46, v46, v114, s[28:29]
	v_cndmask_b32_e64 v47, v47, v114, s[30:31]
	v_cndmask_b32_e64 v48, v48, v114, s[34:35]
	v_cndmask_b32_e64 v49, v49, v114, s[36:37]
.LBB2_17:
	s_nop 8
	v_max_f32_e32 v98, v35, v35
	v_max_f32_e32 v99, v34, v34
	v_max_f32_e32 v98, v99, v98
	v_max3_f32 v98, v98, v36, v37
	v_max3_f32 v98, v98, v38, v39
	v_max3_f32 v98, v98, v40, v41
	v_max3_f32 v98, v98, v42, v43
	v_max3_f32 v98, v98, v44, v45
	v_max3_f32 v98, v98, v46, v47
	v_max3_f32 v98, v98, v48, v49
	ds_bpermute_b32 v99, v138, v98
	s_waitcnt lgkmcnt(0)
	v_max3_f32 v135, v115, v98, v99
	v_sub_f32_e32 v34, v34, v135
	v_sub_f32_e32 v35, v35, v135
	v_exp_f32_e32 v99, v34
	v_exp_f32_e32 v100, v35
	v_sub_f32_e32 v36, v36, v135
	v_sub_f32_e32 v34, v37, v135
	v_exp_f32_e32 v35, v36
	v_add_f32_e32 v36, 0, v99
	v_exp_f32_e32 v101, v34
	v_sub_f32_e32 v34, v38, v135
	v_exp_f32_e32 v38, v34
	v_add_f32_e32 v34, v100, v36
	v_sub_f32_e32 v36, v39, v135
	v_exp_f32_e32 v36, v36
	v_sub_f32_e32 v37, v40, v135
	v_add_f32_e32 v34, v35, v34
	v_exp_f32_e32 v37, v37
	v_sub_f32_e32 v39, v41, v135
	v_add_f32_e32 v34, v101, v34
	v_exp_f32_e32 v39, v39
	v_sub_f32_e32 v40, v42, v135
	v_add_f32_e32 v34, v38, v34
	v_exp_f32_e32 v42, v40
	v_sub_f32_e32 v40, v43, v135
	v_add_f32_e32 v34, v36, v34
	v_exp_f32_e32 v43, v40
	v_sub_f32_e32 v40, v44, v135
	v_add_f32_e32 v34, v37, v34
	v_exp_f32_e32 v44, v40
	v_sub_f32_e32 v40, v45, v135
	v_add_f32_e32 v34, v39, v34
	v_exp_f32_e32 v45, v40
	v_sub_f32_e32 v40, v46, v135
	v_add_f32_e32 v34, v42, v34
	v_exp_f32_e32 v40, v40
	v_add_f32_e32 v34, v43, v34
	v_add_f32_e32 v34, v44, v34
	v_add_f32_e32 v34, v45, v34
	v_add_f32_e32 v41, v40, v34
	v_sub_f32_e32 v34, v47, v135
	v_exp_f32_e32 v46, v34
	v_sub_f32_e32 v34, v48, v135
	v_exp_f32_e32 v47, v34
	v_sub_f32_e32 v34, v49, v135
	v_sub_f32_e32 v98, v115, v135
	v_exp_f32_e32 v48, v34
	v_exp_f32_e32 v34, v98
	v_add_f32_e32 v41, v46, v41
	v_add_f32_e32 v41, v47, v41
	v_add_f32_e32 v134, v48, v41
	v_fmac_f32_e32 v134, v131, v34
	v_mul_f32_e32 v32, v34, v32
	v_mul_f32_e32 v33, v34, v33
	v_mul_f32_e32 v30, v34, v30
	v_mul_f32_e32 v31, v34, v31
	v_mul_f32_e32 v28, v34, v28
	v_mul_f32_e32 v29, v34, v29
	v_mul_f32_e32 v26, v34, v26
	v_mul_f32_e32 v27, v34, v27
	v_mul_f32_e32 v24, v34, v24
	v_mul_f32_e32 v25, v34, v25
	v_mul_f32_e32 v22, v34, v22
	v_mul_f32_e32 v23, v34, v23
	v_mul_f32_e32 v20, v34, v20
	v_mul_f32_e32 v21, v34, v21
	v_mul_f32_e32 v18, v34, v18
	v_mul_f32_e32 v19, v34, v19
	v_mul_f32_e32 v16, v34, v16
	v_mul_f32_e32 v17, v34, v17
	v_mul_f32_e32 v14, v34, v14
	v_mul_f32_e32 v15, v34, v15
	v_mul_f32_e32 v12, v34, v12
	v_mul_f32_e32 v13, v34, v13
	v_mul_f32_e32 v10, v34, v10
	v_mul_f32_e32 v11, v34, v11
	v_mul_f32_e32 v8, v34, v8
	v_mul_f32_e32 v9, v34, v9
	v_mul_f32_e32 v6, v34, v6
	v_mul_f32_e32 v7, v34, v7
	v_mul_f32_e32 v4, v34, v4
	v_mul_f32_e32 v5, v34, v5
	v_mul_f32_e32 v2, v34, v2
	v_mul_f32_e32 v3, v34, v3
	v_cvt_pk_f16_f32 v37, v37, v39
	v_cvt_pk_f16_f32 v36, v38, v36
	v_cvt_pk_f16_f32 v35, v35, v101
	v_cvt_pk_f16_f32 v34, v99, v100
	v_cvt_pk_f16_f32 v41, v47, v48
	v_cvt_pk_f16_f32 v40, v40, v46
	v_cvt_pk_f16_f32 v39, v44, v45
	v_cvt_pk_f16_f32 v38, v42, v43
	s_setprio 3
	s_waitcnt vmcnt(3)
	v_mfma_f32_32x32x16_f16 v[18:33], v[94:97], v[34:37], v[18:33]
	s_waitcnt vmcnt(1)
	v_mfma_f32_32x32x16_f16 v[2:17], v[86:89], v[34:37], v[2:17]
	v_mfma_f32_32x32x16_f16 v[18:33], v[90:93], v[38:41], v[18:33]
	s_waitcnt vmcnt(0)
	v_mfma_f32_32x32x16_f16 v[2:17], v[82:85], v[38:41], v[2:17]
	s_setprio 2
	s_add_i32 s46, s46, 1
	s_add_u32 s2, s2, 0x1000
	s_addc_u32 s3, s3, 0
	s_add_i32 s50, s45, s2
	s_cmp_lg_u32 s50, 0
	s_cbranch_scc0 .LBB2_19
	v_mov_b64_e32 v[100:101], v[68:69]
	v_mov_b64_e32 v[104:105], v[72:73]
	v_mov_b64_e32 v[108:109], v[76:77]
	v_mov_b64_e32 v[34:35], v[78:79]
	v_mov_b32_e32 v115, v135
	v_mov_b32_e32 v131, v134
	v_mov_b64_e32 v[98:99], v[66:67]
	v_mov_b64_e32 v[102:103], v[70:71]
	v_mov_b64_e32 v[106:107], v[74:75]
	v_mov_b64_e32 v[36:37], v[80:81]
	s_branch .LBB2_13

.LBB2_20:
	s_setprio 0
	s_or_b64 exec, exec, s[48:49]
	s_load_dwordx2 s[0:1], s[0:1], 0x18
	v_mul_u32_u24_e32 v34, 0x600, v133
	v_lshlrev_b32_e32 v34, 4, v34
	v_mov_b32_e32 v35, 0
	s_waitcnt lgkmcnt(0)
	v_lshl_add_u64 v[36:37], s[0:1], 0, v[34:35]
	v_mov_b32_e32 v131, v35
	v_lshl_add_u64 v[136:137], v[36:37], 0, v[130:131]
	s_and_saveexec_b64 s[0:1], s[38:39]
	s_cbranch_execz .LBB2_22
	v_add_co_u32_e32 v34, vcc, 0x4000, v136
	s_nop 1
	v_addc_co_u32_e32 v35, vcc, 0, v137, vcc
	global_load_dwordx4 v[126:129], v[34:35], off
	global_load_dwordx4 v[122:125], v[34:35], off offset:1024
	global_load_dwordx4 v[118:121], v[34:35], off offset:2048
	global_load_dwordx4 v[110:113], v[34:35], off offset:3072
	v_add_co_u32_e32 v34, vcc, 0x5000, v136
	s_nop 1
	v_addc_co_u32_e32 v35, vcc, 0, v137, vcc
	global_load_dwordx4 v[114:117], v[34:35], off
	global_load_dwordx4 v[106:109], v[34:35], off offset:1024
	global_load_dwordx4 v[102:105], v[34:35], off offset:2048
	global_load_dwordx4 v[98:101], v[34:35], off offset:3072
